# stream block moved behind the 15th of 16 PV MFMAs (later counted wait for the K/V pieces)
# speedup vs baseline: 1.0107x; 1.0045x over previous
; #define LAS __attribute__((address_space(3)))
; __device__ __forceinline__ unsigned pk2(float lo, float hi) { return f2bf(lo) | (f2bf(hi) << 16); }
;     __device__ __forceinline__ const float* x() const { return (const float*)ld(0); }
;     __device__ __forceinline__ const float* c() const { return (const float*)ld(1); }
; template <bool NT = true> __device__ __forceinline__ void cvt_store(const CvtItem& d, const f32x4 (&v)[8], LAS float* scr, int lane) {
;     const int rr = lane >> 3, c4 = (lane & 7) * 4;
; #pragma unroll
;     for (int q = 0; q < 8; ++q) { LAS float* t = scr + (8 * q + rr) * 33 + c4; t[0] = v[q].x; t[1] = v[q].y; t[2] = v[q].z; t[3] = v[q].w; }
;     asm volatile("s_waitcnt lgkmcnt(0)" ::: "memory");
;     const int c = lane & 7;
; #pragma unroll
;     for (int j = 0; j < 4; ++j) { const int n = (lane >> 3) + 8 * j; const LAS float* s = scr + (8 * c) * 33 + n;
;         u32x4 o; o.x = pk2(s[0 * 33], s[1 * 33]); o.y = pk2(s[2 * 33], s[3 * 33]); o.z = pk2(s[4 * 33], s[5 * 33]); o.w = pk2(s[6 * 33], s[7 * 33]);
;         const int ng = d.n0 + n, drow = d.row_off + (d.ilv ? ((ng >> 7) * 256 + (ng & 127)) : ng);
;         if (NT) __builtin_nontemporal_store(o, (u32x4*)(d.dst + (size_t)drow * d.K + d.k0 + 8 * c)); else *(u32x4*)(d.dst + (size_t)drow * d.K + d.k0 + 8 * c) = o; }
;     asm volatile("s_waitcnt lgkmcnt(0)" ::: "memory");
.LBB0_529:
	v_mfma_f32_32x32x16_bf16 v[66:81], v[194:197], v[134:137], v[66:81]
	v_exp_f32_e32 v162, v162
	v_exp_f32_e32 v163, v163
	ds_read_b64_tr_b16 v[122:123], v16 offset:50176
	ds_read_b64_tr_b16 v[124:125], v16 offset:50688
	s_add_u32 s58, s33, 0xfef80000
	s_addc_u32 s59, s53, -1
	s_add_u32 s2, s33, 0xfefe0000
	s_addc_u32 s3, s53, -1
	s_add_i32 s60, s57, s49
	s_mov_b32 s61, m0
	s_mov_b32 m0, s60
	s_nop 0
	global_load_lds_dwordx4 v237, s[2:3] offset:0
	s_mov_b32 m0, s61
	v_mfma_f32_32x32x16_bf16 v[82:97], v[194:197], v[130:133], v[82:97]
	v_exp_f32_e32 v164, v164
	v_exp_f32_e32 v165, v165
	ds_read_b64_tr_b16 v[126:127], v16 offset:54272
	ds_read_b64_tr_b16 v[128:129], v16 offset:54784
	s_waitcnt lgkmcnt(6)
	v_mfma_f32_32x32x16_bf16 v[34:49], v[194:197], v[118:121], v[34:49]
	v_exp_f32_e32 v166, v166
	v_exp_f32_e32 v167, v167
	ds_read_b64_tr_b16 v[130:131], v16 offset:58368
	ds_read_b64_tr_b16 v[132:133], v16 offset:58880
	s_add_u32 s2, s33, 0xfefe0080
	s_addc_u32 s3, s53, -1
	s_add_i32 s60, s57, s54
	s_mov_b32 s61, m0
	s_mov_b32 m0, s60
	s_nop 0
	global_load_lds_dwordx4 v237, s[2:3] offset:0
	s_mov_b32 m0, s61
	s_waitcnt lgkmcnt(6)
	v_mfma_f32_32x32x16_bf16 v[50:65], v[194:197], v[114:117], v[50:65]
	v_exp_f32_e32 v168, v168
	v_exp_f32_e32 v169, v169
	ds_read_b64_tr_b16 v[118:119], v16 offset:62464
	ds_read_b64_tr_b16 v[120:121], v16 offset:62976
	v_add_u32_e32 v17, s55, v236
	ds_read_b128 v[114:117], v17
	ds_read_b128 v[178:181], v17 offset:512
	s_waitcnt lgkmcnt(8)
	v_mfma_f32_32x32x16_bf16 v[66:81], v[12:15], v[122:125], v[66:81]
	v_exp_f32_e32 v170, v170
	v_exp_f32_e32 v171, v171
	ds_read_b64_tr_b16 v[134:135], v16 offset:51200
	ds_read_b64_tr_b16 v[136:137], v16 offset:51712
	s_add_u32 s2, s33, 0x20000
	s_addc_u32 s3, s53, 0
	s_add_i32 s60, s55, s46
	s_mov_b32 s61, m0
	s_mov_b32 m0, s60
	s_nop 0
	global_load_lds_dwordx4 v235, s[2:3] offset:0
	s_mov_b32 m0, s61
	s_waitcnt lgkmcnt(8)
	v_mfma_f32_32x32x16_bf16 v[82:97], v[12:15], v[126:129], v[82:97]
	v_exp_f32_e32 v172, v172
	v_exp_f32_e32 v173, v173
	ds_read_b64_tr_b16 v[122:123], v16 offset:55296
	ds_read_b64_tr_b16 v[124:125], v16 offset:55808
	ds_read_b128 v[198:201], v17 offset:2048
	ds_read_b128 v[186:189], v17 offset:2560
	s_waitcnt lgkmcnt(10)
	v_mfma_f32_32x32x16_bf16 v[34:49], v[12:15], v[130:133], v[34:49]
	v_exp_f32_e32 v174, v174
	v_exp_f32_e32 v175, v175
	ds_read_b64_tr_b16 v[126:127], v16 offset:59392
	ds_read_b64_tr_b16 v[128:129], v16 offset:59904
	s_add_u32 s2, s33, 0x20080
	s_addc_u32 s3, s53, 0
	s_add_i32 s60, s55, s45
	s_mov_b32 s61, m0
	s_mov_b32 m0, s60
	s_nop 0
	global_load_lds_dwordx4 v235, s[2:3] offset:0
	s_mov_b32 m0, s61
	s_waitcnt lgkmcnt(10)
	v_mfma_f32_32x32x16_bf16 v[50:65], v[12:15], v[118:121], v[50:65]
	v_exp_f32_e32 v176, v176
	v_exp_f32_e32 v177, v177
	ds_read_b64_tr_b16 v[130:131], v16 offset:63488
	ds_read_b64_tr_b16 v[132:133], v16 offset:64000
	ds_read_b128 v[206:209], v17 offset:4096
	ds_read_b128 v[190:193], v17 offset:4608
	s_waitcnt lgkmcnt(10)
	v_mfma_f32_32x32x16_bf16 v[66:81], v[8:11], v[134:137], v[66:81]
	v_exp_f32_e32 v146, v146
	v_exp_f32_e32 v147, v147
	ds_read_b64_tr_b16 v[118:119], v16 offset:52224
	ds_read_b64_tr_b16 v[120:121], v16 offset:52736
	s_waitcnt lgkmcnt(10)
	v_mfma_f32_32x32x16_bf16 v[82:97], v[8:11], v[122:125], v[82:97]
	v_exp_f32_e32 v148, v148
	v_exp_f32_e32 v149, v149
	ds_read_b64_tr_b16 v[134:135], v16 offset:56320
	ds_read_b64_tr_b16 v[136:137], v16 offset:56832
	ds_read_b128 v[202:205], v17 offset:6144
	ds_read_b128 v[182:185], v17 offset:6656
	s_waitcnt lgkmcnt(10)
	v_mfma_f32_32x32x16_bf16 v[34:49], v[8:11], v[126:129], v[34:49]
	v_exp_f32_e32 v150, v150
	v_exp_f32_e32 v151, v151
	ds_read_b64_tr_b16 v[122:123], v16 offset:60416
	ds_read_b64_tr_b16 v[124:125], v16 offset:60928
	s_waitcnt lgkmcnt(10)
	v_mfma_f32_32x32x16_bf16 v[50:65], v[8:11], v[130:133], v[50:65]
	v_exp_f32_e32 v152, v152
	v_exp_f32_e32 v153, v153
	ds_read_b64_tr_b16 v[126:127], v16 offset:64512
	ds_read_b64_tr_b16 v[128:129], v16 offset:65024
	s_waitcnt lgkmcnt(8)
	v_mfma_f32_32x32x16_bf16 v[66:81], v[4:7], v[118:121], v[66:81]
	v_exp_f32_e32 v154, v154
	v_exp_f32_e32 v155, v155
	s_waitcnt lgkmcnt(6)
	v_mfma_f32_32x32x16_bf16 v[82:97], v[4:7], v[134:137], v[82:97]
	v_exp_f32_e32 v156, v156
	v_exp_f32_e32 v157, v157
	s_waitcnt lgkmcnt(2)
	v_mfma_f32_32x32x16_bf16 v[34:49], v[4:7], v[122:125], v[34:49]
	v_exp_f32_e32 v158, v158
	v_exp_f32_e32 v159, v159
	s_add_i32 s2, s56, 1
	s_cmp_gt_i32 s2, s90
	s_cbranch_scc1 .Lcs_done_h0
	s_waitcnt vmcnt(6)
	v_cvt_pk_bf16_f32 v245, v250, v251
	v_cvt_pk_bf16_f32 v244, v252, v253
	s_cmp_lt_u32 s2, 7
	s_cbranch_scc1 .Lcs_dumS_h0
	s_bitcmp1_b32 s2, 1
	s_cbranch_scc1 .Lcs_Sb_h0
	global_store_dwordx2 v28, v[30:31], s[100:101] nt
	v_add_u32_e32 v28, s63, v28

; #define LAS __attribute__((address_space(3)))
; __device__ __forceinline__ unsigned pk2(float lo, float hi) { return f2bf(lo) | (f2bf(hi) << 16); }
;     __device__ __forceinline__ const float* x() const { return (const float*)ld(0); }
;     __device__ __forceinline__ const float* c() const { return (const float*)ld(1); }
; template <bool NT = true> __device__ __forceinline__ void cvt_store(const CvtItem& d, const f32x4 (&v)[8], LAS float* scr, int lane) {
;     const int rr = lane >> 3, c4 = (lane & 7) * 4;
; #pragma unroll
;     for (int q = 0; q < 8; ++q) { LAS float* t = scr + (8 * q + rr) * 33 + c4; t[0] = v[q].x; t[1] = v[q].y; t[2] = v[q].z; t[3] = v[q].w; }
;     asm volatile("s_waitcnt lgkmcnt(0)" ::: "memory");
;     const int c = lane & 7;
; #pragma unroll
;     for (int j = 0; j < 4; ++j) { const int n = (lane >> 3) + 8 * j; const LAS float* s = scr + (8 * c) * 33 + n;
;         u32x4 o; o.x = pk2(s[0 * 33], s[1 * 33]); o.y = pk2(s[2 * 33], s[3 * 33]); o.z = pk2(s[4 * 33], s[5 * 33]); o.w = pk2(s[6 * 33], s[7 * 33]);
;         const int ng = d.n0 + n, drow = d.row_off + (d.ilv ? ((ng >> 7) * 256 + (ng & 127)) : ng);
;         if (NT) __builtin_nontemporal_store(o, (u32x4*)(d.dst + (size_t)drow * d.K + d.k0 + 8 * c)); else *(u32x4*)(d.dst + (size_t)drow * d.K + d.k0 + 8 * c) = o; }
;     asm volatile("s_waitcnt lgkmcnt(0)" ::: "memory");
.Lcs_noL_h0:
	s_waitcnt lgkmcnt(0)
	v_mfma_f32_32x32x16_bf16 v[50:65], v[4:7], v[126:129], v[50:65]
	v_exp_f32_e32 v160, v160
	v_exp_f32_e32 v161, v161
	s_waitcnt lgkmcnt(0)
	s_cmp_gt_i32 s2, s90
	s_cbranch_scc1 .Lcs_noW_h0
	s_bitcmp1_b32 s2, 1
	s_cbranch_scc1 .Lcs_R_h0

; #define LAS __attribute__((address_space(3)))
; __device__ __forceinline__ unsigned pk2(float lo, float hi) { return f2bf(lo) | (f2bf(hi) << 16); }
;     __device__ __forceinline__ const float* x() const { return (const float*)ld(0); }
;     __device__ __forceinline__ const float* c() const { return (const float*)ld(1); }
; template <bool NT = true> __device__ __forceinline__ void cvt_store(const CvtItem& d, const f32x4 (&v)[8], LAS float* scr, int lane) {
;     const int rr = lane >> 3, c4 = (lane & 7) * 4;
; #pragma unroll
;     for (int q = 0; q < 8; ++q) { LAS float* t = scr + (8 * q + rr) * 33 + c4; t[0] = v[q].x; t[1] = v[q].y; t[2] = v[q].z; t[3] = v[q].w; }
;     asm volatile("s_waitcnt lgkmcnt(0)" ::: "memory");
;     const int c = lane & 7;
; #pragma unroll
;     for (int j = 0; j < 4; ++j) { const int n = (lane >> 3) + 8 * j; const LAS float* s = scr + (8 * c) * 33 + n;
;         u32x4 o; o.x = pk2(s[0 * 33], s[1 * 33]); o.y = pk2(s[2 * 33], s[3 * 33]); o.z = pk2(s[4 * 33], s[5 * 33]); o.w = pk2(s[6 * 33], s[7 * 33]);
;         const int ng = d.n0 + n, drow = d.row_off + (d.ilv ? ((ng >> 7) * 256 + (ng & 127)) : ng);
;         if (NT) __builtin_nontemporal_store(o, (u32x4*)(d.dst + (size_t)drow * d.K + d.k0 + 8 * c)); else *(u32x4*)(d.dst + (size_t)drow * d.K + d.k0 + 8 * c) = o; }
;     asm volatile("s_waitcnt lgkmcnt(0)" ::: "memory");
.LBB0_532:
	s_add_i32 s2, s55, 0x4000
	s_cmpk_lg_u32 s55, 0x8000
	s_cselect_b32 s57, s2, 0
	v_mfma_f32_32x32x16_bf16 v[66:81], v[194:197], v[166:169], v[66:81]
	v_exp_f32_e32 v130, v130
	v_exp_f32_e32 v131, v131
	ds_read_b64_tr_b16 v[154:155], v16 offset:50176
	ds_read_b64_tr_b16 v[156:157], v16 offset:50688
	s_add_u32 s2, s58, 0x80000
	s_addc_u32 s3, s59, 0
	s_add_i32 s60, s55, s49
	s_mov_b32 s61, m0
	s_mov_b32 m0, s60
	s_nop 0
	global_load_lds_dwordx4 v237, s[2:3] offset:0
	s_mov_b32 m0, s61
	v_mfma_f32_32x32x16_bf16 v[82:97], v[194:197], v[162:165], v[82:97]
	v_exp_f32_e32 v132, v132
	v_exp_f32_e32 v133, v133
	ds_read_b64_tr_b16 v[158:159], v16 offset:54272
	ds_read_b64_tr_b16 v[160:161], v16 offset:54784
	s_waitcnt lgkmcnt(6)
	v_mfma_f32_32x32x16_bf16 v[34:49], v[194:197], v[150:153], v[34:49]
	v_exp_f32_e32 v134, v134
	v_exp_f32_e32 v135, v135
	ds_read_b64_tr_b16 v[162:163], v16 offset:58368
	ds_read_b64_tr_b16 v[164:165], v16 offset:58880
	s_add_u32 s2, s58, 0x80080
	s_addc_u32 s3, s59, 0
	s_add_i32 s58, s55, s54
	s_mov_b32 s59, m0
	s_mov_b32 m0, s58
	s_nop 0
	global_load_lds_dwordx4 v237, s[2:3] offset:0
	s_mov_b32 m0, s59
	s_waitcnt lgkmcnt(6)
	v_mfma_f32_32x32x16_bf16 v[50:65], v[194:197], v[146:149], v[50:65]
	v_exp_f32_e32 v136, v136
	v_exp_f32_e32 v137, v137
	ds_read_b64_tr_b16 v[150:151], v16 offset:62464
	ds_read_b64_tr_b16 v[152:153], v16 offset:62976
	v_add_u32_e32 v3, s57, v236
	ds_read_b128 v[146:149], v3
	ds_read_b128 v[202:205], v3 offset:512
	s_waitcnt lgkmcnt(8)
	v_mfma_f32_32x32x16_bf16 v[66:81], v[12:15], v[154:157], v[66:81]
	v_exp_f32_e32 v138, v138
	v_exp_f32_e32 v139, v139
	ds_read_b64_tr_b16 v[166:167], v16 offset:51200
	ds_read_b64_tr_b16 v[168:169], v16 offset:51712
	s_add_u32 s2, s33, 0x40000
	s_addc_u32 s3, s53, 0
	s_add_i32 s58, s57, s46
	s_mov_b32 s59, m0
	s_mov_b32 m0, s58
	s_nop 0
	global_load_lds_dwordx4 v235, s[2:3] offset:0
	s_mov_b32 m0, s59
	s_waitcnt lgkmcnt(8)
	v_mfma_f32_32x32x16_bf16 v[82:97], v[12:15], v[158:161], v[82:97]
	v_exp_f32_e32 v140, v140
	v_exp_f32_e32 v141, v141
	ds_read_b64_tr_b16 v[154:155], v16 offset:55296
	ds_read_b64_tr_b16 v[156:157], v16 offset:55808
	ds_read_b128 v[206:209], v3 offset:2048
	ds_read_b128 v[190:193], v3 offset:2560
	s_waitcnt lgkmcnt(10)
	v_mfma_f32_32x32x16_bf16 v[34:49], v[12:15], v[162:165], v[34:49]
	v_exp_f32_e32 v142, v142
	v_exp_f32_e32 v143, v143
	ds_read_b64_tr_b16 v[158:159], v16 offset:59392
	ds_read_b64_tr_b16 v[160:161], v16 offset:59904
	s_add_u32 s2, s33, 0x40080
	s_addc_u32 s3, s53, 0
	s_add_i32 s58, s57, s45
	s_mov_b32 s59, m0
	s_mov_b32 m0, s58
	s_nop 0
	global_load_lds_dwordx4 v235, s[2:3] offset:0
	s_mov_b32 m0, s59
	s_waitcnt lgkmcnt(10)
	v_mfma_f32_32x32x16_bf16 v[50:65], v[12:15], v[150:153], v[50:65]
	v_exp_f32_e32 v144, v144
	v_exp_f32_e32 v145, v145
	ds_read_b64_tr_b16 v[162:163], v16 offset:63488
	ds_read_b64_tr_b16 v[164:165], v16 offset:64000
	ds_read_b128 v[198:201], v3 offset:4096
	ds_read_b128 v[186:189], v3 offset:4608
	s_waitcnt lgkmcnt(10)
	v_mfma_f32_32x32x16_bf16 v[66:81], v[8:11], v[166:169], v[66:81]
	v_exp_f32_e32 v114, v114
	v_exp_f32_e32 v115, v115
	ds_read_b64_tr_b16 v[150:151], v16 offset:52224
	ds_read_b64_tr_b16 v[152:153], v16 offset:52736
	s_waitcnt lgkmcnt(10)
	v_mfma_f32_32x32x16_bf16 v[82:97], v[8:11], v[154:157], v[82:97]
	v_exp_f32_e32 v116, v116
	v_exp_f32_e32 v117, v117
	ds_read_b64_tr_b16 v[166:167], v16 offset:56320
	ds_read_b64_tr_b16 v[168:169], v16 offset:56832
	ds_read_b128 v[182:185], v3 offset:6144
	ds_read_b128 v[178:181], v3 offset:6656
	s_waitcnt lgkmcnt(10)
	v_mfma_f32_32x32x16_bf16 v[34:49], v[8:11], v[158:161], v[34:49]
	v_exp_f32_e32 v118, v118
	v_exp_f32_e32 v119, v119
	ds_read_b64_tr_b16 v[154:155], v16 offset:60416
	ds_read_b64_tr_b16 v[156:157], v16 offset:60928
	s_waitcnt lgkmcnt(10)
	v_mfma_f32_32x32x16_bf16 v[50:65], v[8:11], v[162:165], v[50:65]
	v_exp_f32_e32 v120, v120
	v_exp_f32_e32 v121, v121
	ds_read_b64_tr_b16 v[158:159], v16 offset:64512
	ds_read_b64_tr_b16 v[160:161], v16 offset:65024
	s_waitcnt lgkmcnt(8)
	v_mfma_f32_32x32x16_bf16 v[66:81], v[4:7], v[150:153], v[66:81]
	v_exp_f32_e32 v122, v122
	v_exp_f32_e32 v123, v123
	s_waitcnt lgkmcnt(6)
	v_mfma_f32_32x32x16_bf16 v[82:97], v[4:7], v[166:169], v[82:97]
	v_exp_f32_e32 v124, v124
	v_exp_f32_e32 v125, v125
	s_waitcnt lgkmcnt(2)
	v_mfma_f32_32x32x16_bf16 v[34:49], v[4:7], v[154:157], v[34:49]
	v_exp_f32_e32 v126, v126
	v_exp_f32_e32 v127, v127
	s_add_i32 s2, s56, 2
	s_cmp_gt_i32 s2, s90
	s_cbranch_scc1 .Lcs_done_h1
	s_waitcnt vmcnt(6)
	v_cvt_pk_bf16_f32 v245, v18, v19
	v_cvt_pk_bf16_f32 v244, v20, v21
	s_cmp_lt_u32 s2, 7
	s_cbranch_scc1 .Lcs_dumS_h1
	s_and_b32 s61, s2, 7
	s_cmp_eq_u32 s61, 7
	s_cbranch_scc1 .Lcs_adopt_h1

; #define LAS __attribute__((address_space(3)))
; __device__ __forceinline__ unsigned pk2(float lo, float hi) { return f2bf(lo) | (f2bf(hi) << 16); }
;     __device__ __forceinline__ const float* x() const { return (const float*)ld(0); }
;     __device__ __forceinline__ const float* c() const { return (const float*)ld(1); }
; template <bool NT = true> __device__ __forceinline__ void cvt_store(const CvtItem& d, const f32x4 (&v)[8], LAS float* scr, int lane) {
;     const int rr = lane >> 3, c4 = (lane & 7) * 4;
; #pragma unroll
;     for (int q = 0; q < 8; ++q) { LAS float* t = scr + (8 * q + rr) * 33 + c4; t[0] = v[q].x; t[1] = v[q].y; t[2] = v[q].z; t[3] = v[q].w; }
;     asm volatile("s_waitcnt lgkmcnt(0)" ::: "memory");
;     const int c = lane & 7;
; #pragma unroll
;     for (int j = 0; j < 4; ++j) { const int n = (lane >> 3) + 8 * j; const LAS float* s = scr + (8 * c) * 33 + n;
;         u32x4 o; o.x = pk2(s[0 * 33], s[1 * 33]); o.y = pk2(s[2 * 33], s[3 * 33]); o.z = pk2(s[4 * 33], s[5 * 33]); o.w = pk2(s[6 * 33], s[7 * 33]);
;         const int ng = d.n0 + n, drow = d.row_off + (d.ilv ? ((ng >> 7) * 256 + (ng & 127)) : ng);
;         if (NT) __builtin_nontemporal_store(o, (u32x4*)(d.dst + (size_t)drow * d.K + d.k0 + 8 * c)); else *(u32x4*)(d.dst + (size_t)drow * d.K + d.k0 + 8 * c) = o; }
;     asm volatile("s_waitcnt lgkmcnt(0)" ::: "memory");
.Lcs_noL_h1:
	s_waitcnt lgkmcnt(0)
	v_mfma_f32_32x32x16_bf16 v[50:65], v[4:7], v[158:161], v[50:65]
	v_exp_f32_e32 v128, v128
	v_exp_f32_e32 v129, v129
	s_waitcnt lgkmcnt(0)
	s_cmp_gt_i32 s2, s90
	s_cbranch_scc1 .Lcs_noW_h1
	ds_write_b16 v29, v245
	ds_write_b16_d16_hi v29, v245 offset:64
	ds_write_b16 v29, v244 offset:128
	ds_write_b16_d16_hi v29, v244 offset:192
	s_bitcmp1_b32 s2, 1
	s_cselect_b32 s3, 16, -48
	v_add_u32_e32 v29, s3, v29
